# baseline (speedup 1.0000x reference)
.LBB3_6:
	s_or_b64 exec, exec, s[24:25]
	s_or_b32 s24, s16, 8
	s_ashr_i32 s25, s24, 31
	s_lshl_b64 s[24:25], s[24:25], 16
	s_add_u32 s9, s6, s24
	s_addc_u32 s16, s7, s25
	s_add_u32 s24, s9, s17
	s_addc_u32 s25, s16, 0
	s_add_i32 s9, 0, 0x18000
	s_add_i32 s16, s9, s31
	v_mov_b32_e32 v3, v140
	s_mov_b32 m0, s16
	v_mov_b32_e32 v130, v140
	s_waitcnt vmcnt(4)
	s_barrier
	s_add_i32 s51, s43, 0x8000
	global_load_lds_dwordx4 v3, s[24:25] sc0
	s_add_i32 m0, s16, 0x2000
	v_lshl_add_u64 v[4:5], s[24:25], 0, v[130:131]
	v_lshl_add_u64 v[4:5], v[4:5], 0, s[18:19]
	v_mov_b32_e32 v130, v1
	global_load_lds_dwordx4 v[4:5], off sc0
	s_mov_b64 s[18:19], 0x80
	v_lshl_add_u64 v[4:5], s[14:15], 0, v[130:131]
	v_lshl_add_u64 v[4:5], v[4:5], 0, s[18:19]
	s_mov_b32 m0, s51
	v_mov_b32_e32 v130, v1
	global_load_lds_dwordx4 v[4:5], off
	s_add_i32 s52, s43, 0xa000
	v_lshl_add_u64 v[4:5], s[14:15], 0, v[130:131]
	s_mov_b64 s[14:15], 0x10080
	v_lshl_add_u64 v[4:5], v[4:5], 0, s[14:15]
	s_mov_b32 m0, s52
	s_add_i32 s14, 0, 0x1c000
	v_mov_b32_e32 v130, v140
	global_load_lds_dwordx4 v[4:5], off
	s_add_i32 s15, s14, s31
	s_mov_b32 m0, s15
	v_lshl_add_u64 v[4:5], s[24:25], 0, v[130:131]
	v_lshl_add_u64 v[4:5], v[4:5], 0, s[20:21]
	v_mov_b32_e32 v130, v140
	global_load_lds_dwordx4 v[4:5], off sc0
	s_add_i32 m0, s15, 0x2000
	v_lshl_add_u64 v[4:5], s[24:25], 0, v[130:131]
	v_lshl_add_u64 v[4:5], v[4:5], 0, s[22:23]
	global_load_lds_dwordx4 v[4:5], off sc0
	v_lshlrev_b32_e32 v4, 6, v0
	v_lshlrev_b32_e32 v6, 2, v0
	v_and_b32_e32 v3, 48, v0
	v_and_b32_e32 v5, 0x3c0, v4
	v_and_b32_e32 v6, 32, v6
	v_bitop3_b32 v3, v3, v6, v5 bitop3:0x36
	v_add_u32_e32 v7, s9, v3
	s_lshl_b32 s9, s28, 3
	s_add_i32 s26, s26, s9
	s_sub_i32 s9, s26, s30
	v_add_u32_e32 v8, s14, v3
	s_sub_i32 s9, s9, s29
	s_lshl_b32 s14, s27, 3
	s_add_i32 s15, 0, 0x10000
	s_sub_i32 s9, s9, s14
	v_add_u32_e32 v5, s15, v3
	s_add_i32 s15, 0, 0x14000
	s_lshl_b32 s14, s9, 8
	v_add_u32_e32 v6, s15, v3
	s_ashr_i32 s15, s14, 31
	s_lshl_b64 s[14:15], s[14:15], 10
	s_add_u32 s4, s4, s14
	s_addc_u32 s5, s5, s15
	s_add_u32 s4, s4, 0x30100
	s_addc_u32 s5, s5, 0
	s_add_u32 s9, s12, s17
	s_addc_u32 s12, s13, 0
	s_add_u32 s6, s6, s9
	s_waitcnt vmcnt(6)
	v_lshlrev_b32_e32 v2, 13, v2
	s_addc_u32 s7, s7, s12
	s_waitcnt lgkmcnt(0)
	s_lshl_b32 s56, s8, 2
	s_add_u32 s56, s2, s56
	s_addc_u32 s57, s3, 0
	v_and_b32_e32 v254, 63, v0
	v_lshlrev_b32_e32 v254, 4, v254
	s_mov_b32 m0, 0x20000
	s_nop 0
	global_load_lds_dwordx4 v254, s[56:57]
	v_and_b32_e32 v4, 0x3000, v4
	v_add_u32_e32 v3, 0, v3
	v_or_b32_e32 v9, 0x800, v2
	v_or_b32_e32 v10, 0x1000, v2
	v_or_b32_e32 v11, 0x1800, v2
	s_add_u32 s6, s6, 0x180c00
	s_mov_b32 s12, 0xfffeff80
	s_movk_i32 s14, 0xff80
	s_mov_b32 s16, 0xfff7f400
	s_mov_b32 s18, 0xfff7f800
	s_mov_b32 s20, 0xfffd0000
	s_mov_b32 s22, 0xfffe0000
	s_mov_b32 s24, 0xfff7fc00
	s_mov_b32 s26, 0xfff80000
	s_mov_b32 s28, 0xffff0000
	s_movk_i32 s30, 0xf400
	s_movk_i32 s34, 0xf800
	s_mov_b32 s36, 0xfffd0080
	s_mov_b32 s38, 0xfffe0080
	s_movk_i32 s40, 0xfc00
	s_addc_u32 s7, s7, 0
	s_mov_b32 s53, -2
	v_add_u32_e32 v132, v5, v4
	v_add_u32_e32 v133, v3, v2
	v_add_u32_e32 v134, v3, v9
	v_add_u32_e32 v135, v3, v10
	v_add_u32_e32 v136, v3, v11
	s_mov_b32 s13, -1
	s_add_i32 s9, s43, 0xc000
	s_mov_b32 s15, -1
	s_add_i32 s42, s43, 0xe000
	v_add_u32_e32 v137, v6, v4
	s_mov_b32 s17, -1
	s_mov_b32 s19, -1
	s_mov_b32 s21, -1
	s_mov_b32 s23, -1
	s_mov_b32 s25, -1
	s_mov_b32 s27, -1
	v_add_u32_e32 v138, v7, v4
	s_mov_b32 s29, -1
	v_add_u32_e32 v139, v8, v4
	s_mov_b32 s31, -1
	s_mov_b32 s35, -1
	s_add_i32 s54, s43, 0x1a000
	s_mov_b32 s37, -1
	s_mov_b32 s39, -1
	s_mov_b32 s41, -1
	s_add_i32 s55, s43, 0x1e000
	s_barrier
	ds_read_b128 v[142:145], v132
	ds_read_b128 v[146:149], v132 offset:1024
	ds_read_b128 v[150:153], v132 offset:2048
	ds_read_b128 v[154:157], v132 offset:3072
	v_mov_b32_e32 v130, v1
	ds_read_b128 v[158:161], v133
	ds_read_b128 v[162:165], v133 offset:1024
	ds_read_b128 v[166:169], v134
	ds_read_b128 v[170:173], v134 offset:1024
	ds_read_b128 v[174:177], v135
	ds_read_b128 v[178:181], v135 offset:1024
	ds_read_b128 v[182:185], v136
	ds_read_b128 v[186:189], v136 offset:1024
	s_mov_b32 m0, s9
	v_lshl_add_u64 v[190:191], s[4:5], 0, v[130:131]
	v_lshl_add_u64 v[190:191], v[190:191], 0, s[12:13]
	v_mov_b32_e32 v130, v1
	global_load_lds_dwordx4 v[190:191], off
	s_mov_b32 m0, s42
	v_lshl_add_u64 v[190:191], s[4:5], 0, v[130:131]
	v_lshl_add_u64 v[190:191], v[190:191], 0, s[14:15]
	global_load_lds_dwordx4 v[190:191], off
	s_waitcnt lgkmcnt(8)
	s_barrier
	s_waitcnt lgkmcnt(0)
	s_setprio 3
	s_waitcnt lgkmcnt(0)
	v_mfma_f32_16x16x128_f8f6f4 v[126:129], v[158:165], v[142:149], 0
	v_mfma_f32_16x16x128_f8f6f4 v[122:125], v[158:165], v[150:157], 0
	v_mfma_f32_16x16x128_f8f6f4 v[118:121], v[166:173], v[142:149], 0
	v_mfma_f32_16x16x128_f8f6f4 v[114:117], v[166:173], v[150:157], 0
	v_mfma_f32_16x16x128_f8f6f4 v[190:193], v[174:181], v[142:149], 0
	v_mfma_f32_16x16x128_f8f6f4 v[194:197], v[174:181], v[150:157], 0
	v_mfma_f32_16x16x128_f8f6f4 v[198:201], v[182:189], v[142:149], 0
	v_mfma_f32_16x16x128_f8f6f4 v[202:205], v[182:189], v[150:157], 0
	s_setprio 0
	s_barrier
	v_mov_b32_e32 v130, v140
	s_nop 3
	ds_read_b128 v[82:85], v137
	ds_read_b128 v[86:89], v137 offset:1024
	ds_read_b128 v[90:93], v137 offset:2048
	ds_read_b128 v[94:97], v137 offset:3072
	s_mov_b32 m0, s44
	v_lshl_add_u64 v[206:207], s[6:7], 0, v[130:131]
	v_lshl_add_u64 v[206:207], v[206:207], 0, s[16:17]
	v_mov_b32_e32 v130, v140
	global_load_lds_dwordx4 v[206:207], off sc0
	s_mov_b32 m0, s45
	v_lshl_add_u64 v[206:207], s[6:7], 0, v[130:131]
	v_lshl_add_u64 v[206:207], v[206:207], 0, s[18:19]
	global_load_lds_dwordx4 v[206:207], off sc0
	s_barrier
	s_waitcnt lgkmcnt(0)
	s_setprio 3
	s_waitcnt lgkmcnt(0)
	v_mfma_f32_16x16x128_f8f6f4 v[206:209], v[158:165], v[82:89], 0
	v_mfma_f32_16x16x128_f8f6f4 v[158:161], v[158:165], v[90:97], 0
	v_mfma_f32_16x16x128_f8f6f4 v[162:165], v[166:173], v[82:89], 0
	v_mfma_f32_16x16x128_f8f6f4 v[166:169], v[166:173], v[90:97], 0
	v_mfma_f32_16x16x128_f8f6f4 v[170:173], v[174:181], v[82:89], 0
	v_mfma_f32_16x16x128_f8f6f4 v[174:177], v[174:181], v[90:97], 0
	v_mfma_f32_16x16x128_f8f6f4 v[178:181], v[182:189], v[82:89], 0
	v_mfma_f32_16x16x128_f8f6f4 v[182:185], v[182:189], v[90:97], 0
	s_setprio 0
	v_mov_b32_e32 v130, v1
	s_barrier
	s_nop 3
	ds_read_b128 v[66:69], v133 offset:16384
	ds_read_b128 v[70:73], v133 offset:17408
	ds_read_b128 v[74:77], v134 offset:16384
	ds_read_b128 v[78:81], v134 offset:17408
	ds_read_b128 v[98:101], v135 offset:16384
	ds_read_b128 v[102:105], v135 offset:17408
	ds_read_b128 v[106:109], v136 offset:16384
	ds_read_b128 v[110:113], v136 offset:17408
	s_mov_b32 m0, s43
	v_lshl_add_u64 v[186:187], s[4:5], 0, v[130:131]
	v_lshl_add_u64 v[186:187], v[186:187], 0, s[20:21]
	v_mov_b32_e32 v130, v1
	global_load_lds_dwordx4 v[186:187], off
	s_mov_b32 m0, s46
	v_lshl_add_u64 v[186:187], s[4:5], 0, v[130:131]
	v_lshl_add_u64 v[186:187], v[186:187], 0, s[22:23]
	global_load_lds_dwordx4 v[186:187], off
	s_barrier
	s_waitcnt lgkmcnt(0)
	s_setprio 3
	s_waitcnt lgkmcnt(0)
	v_mfma_f32_16x16x128_f8f6f4 v[62:65], v[66:73], v[142:149], 0
	v_mfma_f32_16x16x128_f8f6f4 v[54:57], v[66:73], v[150:157], 0
	v_mfma_f32_16x16x128_f8f6f4 v[58:61], v[74:81], v[142:149], 0
	v_mfma_f32_16x16x128_f8f6f4 v[50:53], v[74:81], v[150:157], 0
	v_mfma_f32_16x16x128_f8f6f4 v[186:189], v[98:105], v[142:149], 0
	v_mfma_f32_16x16x128_f8f6f4 v[210:213], v[98:105], v[150:157], 0
	v_mfma_f32_16x16x128_f8f6f4 v[214:217], v[106:113], v[142:149], 0
	v_mfma_f32_16x16x128_f8f6f4 v[218:221], v[106:113], v[150:157], 0
	s_setprio 0
	s_barrier
	v_mov_b32_e32 v130, v140
	s_mov_b32 m0, s47
	s_nop 2
	v_lshl_add_u64 v[18:19], s[6:7], 0, v[130:131]
	v_lshl_add_u64 v[18:19], v[18:19], 0, s[24:25]
	v_mov_b32_e32 v130, v140
	global_load_lds_dwordx4 v[18:19], off sc0
	s_mov_b32 m0, s48
	v_lshl_add_u64 v[18:19], s[6:7], 0, v[130:131]
	v_lshl_add_u64 v[18:19], v[18:19], 0, s[26:27]
	global_load_lds_dwordx4 v[18:19], off sc0
	s_waitcnt vmcnt(6)
	s_barrier
	s_setprio 3
	v_mfma_f32_16x16x128_f8f6f4 v[222:225], v[66:73], v[82:89], 0
	v_mfma_f32_16x16x128_f8f6f4 v[226:229], v[66:73], v[90:97], 0
	v_mfma_f32_16x16x128_f8f6f4 v[230:233], v[74:81], v[82:89], 0
	v_mfma_f32_16x16x128_f8f6f4 v[234:237], v[74:81], v[90:97], 0
	v_mfma_f32_16x16x128_f8f6f4 v[238:241], v[98:105], v[82:89], 0
	v_mfma_f32_16x16x128_f8f6f4 v[242:245], v[98:105], v[90:97], 0
	v_mfma_f32_16x16x128_f8f6f4 v[246:249], v[106:113], v[82:89], 0
	v_mfma_f32_16x16x128_f8f6f4 v[250:253], v[106:113], v[90:97], 0
	s_setprio 0
	s_barrier
	s_nop 4
	ds_read_b128 v[2:5], v138
	ds_read_b128 v[6:9], v138 offset:1024
	ds_read_b128 v[10:13], v138 offset:2048
	ds_read_b128 v[14:17], v138 offset:3072
	v_mov_b32_e32 v130, v1
	ds_read_b128 v[18:21], v133 offset:32768
	ds_read_b128 v[22:25], v133 offset:33792
	ds_read_b128 v[26:29], v134 offset:32768
	ds_read_b128 v[30:33], v134 offset:33792
	ds_read_b128 v[34:37], v135 offset:32768
	ds_read_b128 v[38:41], v135 offset:33792
	ds_read_b128 v[42:45], v136 offset:32768
	ds_read_b128 v[46:49], v136 offset:33792
	s_mov_b32 m0, s49
	v_lshl_add_u64 v[66:67], s[4:5], 0, v[130:131]
	v_lshl_add_u64 v[66:67], v[66:67], 0, s[28:29]
	global_load_lds_dwordx4 v[66:67], off
	v_mov_b32_e32 v66, v1
	s_mov_b32 m0, s50
	s_nop 0
	global_load_lds_dwordx4 v66, s[4:5]
	s_waitcnt lgkmcnt(8)
	s_barrier
	s_waitcnt lgkmcnt(0)
	s_setprio 3
	s_waitcnt lgkmcnt(0)
	v_mfma_f32_16x16x128_f8f6f4 v[126:129], v[18:25], v[2:9], v[126:129]
	v_mfma_f32_16x16x128_f8f6f4 v[122:125], v[18:25], v[10:17], v[122:125]
	v_mfma_f32_16x16x128_f8f6f4 v[118:121], v[26:33], v[2:9], v[118:121]
	v_mfma_f32_16x16x128_f8f6f4 v[114:117], v[26:33], v[10:17], v[114:117]
	v_mfma_f32_16x16x128_f8f6f4 v[94:97], v[34:41], v[2:9], v[190:193]
	v_mfma_f32_16x16x128_f8f6f4 v[86:89], v[34:41], v[10:17], v[194:197]
	v_mfma_f32_16x16x128_f8f6f4 v[90:93], v[42:49], v[2:9], v[198:201]
	v_mfma_f32_16x16x128_f8f6f4 v[82:85], v[42:49], v[10:17], v[202:205]
	s_setprio 0
	s_barrier
	v_mov_b32_e32 v130, v140
	ds_read_b128 v[142:145], v139
	ds_read_b128 v[146:149], v139 offset:1024
	ds_read_b128 v[150:153], v139 offset:2048
	ds_read_b128 v[154:157], v139 offset:3072
	s_add_i32 m0, s43, 0x18000
	v_lshl_add_u64 v[66:67], s[6:7], 0, v[130:131]
	v_lshl_add_u64 v[66:67], v[66:67], 0, s[30:31]
	v_mov_b32_e32 v130, v140
	global_load_lds_dwordx4 v[66:67], off sc0
	s_mov_b32 m0, s54
	v_lshl_add_u64 v[66:67], s[6:7], 0, v[130:131]
	v_lshl_add_u64 v[66:67], v[66:67], 0, s[34:35]
	global_load_lds_dwordx4 v[66:67], off sc0
	s_barrier
	s_waitcnt lgkmcnt(0)
	s_setprio 3
	s_waitcnt lgkmcnt(0)
	v_mfma_f32_16x16x128_f8f6f4 v[110:113], v[18:25], v[142:149], v[206:209]
	v_mfma_f32_16x16x128_f8f6f4 v[102:105], v[18:25], v[150:157], v[158:161]
	v_mfma_f32_16x16x128_f8f6f4 v[106:109], v[26:33], v[142:149], v[162:165]
	v_mfma_f32_16x16x128_f8f6f4 v[98:101], v[26:33], v[150:157], v[166:169]
	v_mfma_f32_16x16x128_f8f6f4 v[78:81], v[34:41], v[142:149], v[170:173]
	v_mfma_f32_16x16x128_f8f6f4 v[70:73], v[34:41], v[150:157], v[174:177]
	v_mfma_f32_16x16x128_f8f6f4 v[74:77], v[42:49], v[142:149], v[178:181]
	v_mfma_f32_16x16x128_f8f6f4 v[66:69], v[42:49], v[150:157], v[182:185]
	s_setprio 0
	v_mov_b32_e32 v130, v1
	s_barrier
	ds_read_b128 v[38:41], v133 offset:49152
	ds_read_b128 v[42:45], v133 offset:50176
	ds_read_b128 v[158:161], v134 offset:49152
	ds_read_b128 v[162:165], v134 offset:50176
	ds_read_b128 v[166:169], v135 offset:49152
	ds_read_b128 v[170:173], v135 offset:50176
	ds_read_b128 v[174:177], v136 offset:49152
	ds_read_b128 v[178:181], v136 offset:50176
	s_mov_b32 m0, s51
	v_lshl_add_u64 v[18:19], s[4:5], 0, v[130:131]
	v_lshl_add_u64 v[18:19], v[18:19], 0, s[36:37]
	v_mov_b32_e32 v130, v1
	global_load_lds_dwordx4 v[18:19], off
	s_mov_b32 m0, s52
	v_lshl_add_u64 v[18:19], s[4:5], 0, v[130:131]
	v_lshl_add_u64 v[18:19], v[18:19], 0, s[38:39]
	global_load_lds_dwordx4 v[18:19], off
	s_barrier
	s_waitcnt lgkmcnt(0)
	s_setprio 3
	s_waitcnt lgkmcnt(0)
	v_mfma_f32_16x16x128_f8f6f4 v[62:65], v[38:45], v[2:9], v[62:65]
	v_mfma_f32_16x16x128_f8f6f4 v[54:57], v[38:45], v[10:17], v[54:57]
	v_mfma_f32_16x16x128_f8f6f4 v[58:61], v[158:165], v[2:9], v[58:61]
	v_mfma_f32_16x16x128_f8f6f4 v[50:53], v[158:165], v[10:17], v[50:53]
	v_mfma_f32_16x16x128_f8f6f4 v[34:37], v[166:173], v[2:9], v[186:189]
	v_mfma_f32_16x16x128_f8f6f4 v[22:25], v[166:173], v[10:17], v[210:213]
	v_mfma_f32_16x16x128_f8f6f4 v[26:29], v[174:181], v[2:9], v[214:217]
	v_mfma_f32_16x16x128_f8f6f4 v[18:21], v[174:181], v[10:17], v[218:221]
	s_setprio 0
	s_barrier
	v_mov_b32_e32 v130, v140
	s_add_i32 m0, s43, 0x1c000
	v_lshl_add_u64 v[2:3], s[6:7], 0, v[130:131]
	v_lshl_add_u64 v[2:3], v[2:3], 0, s[40:41]
	global_load_lds_dwordx4 v[2:3], off sc0
	v_mov_b32_e32 v2, v140
	s_mov_b32 m0, s55
	s_nop 0
	global_load_lds_dwordx4 v2, s[6:7] sc0
	s_waitcnt vmcnt(6)
	s_barrier
	s_setprio 3
	v_mfma_f32_16x16x128_f8f6f4 v[46:49], v[38:45], v[142:149], v[222:225]
	v_mfma_f32_16x16x128_f8f6f4 v[38:41], v[38:45], v[150:157], v[226:229]
	v_mfma_f32_16x16x128_f8f6f4 v[42:45], v[158:165], v[142:149], v[230:233]
	v_mfma_f32_16x16x128_f8f6f4 v[30:33], v[158:165], v[150:157], v[234:237]
	v_mfma_f32_16x16x128_f8f6f4 v[14:17], v[166:173], v[142:149], v[238:241]
	v_mfma_f32_16x16x128_f8f6f4 v[6:9], v[166:173], v[150:157], v[242:245]
	v_mfma_f32_16x16x128_f8f6f4 v[10:13], v[174:181], v[142:149], v[246:249]
	v_mfma_f32_16x16x128_f8f6f4 v[2:5], v[174:181], v[150:157], v[250:253]
	s_setprio 0
	s_add_i32 s53, s53, 2
	s_add_u32 s4, s4, 0x100
	s_addc_u32 s5, s5, 0
	s_add_u32 s6, s6, 0x100000
	s_addc_u32 s7, s7, 0
	s_cmp_lt_u32 s53, 4
	s_barrier
